# v55 + RG-LRU phases: one static s_setprio 1 for waves 4-7 (the staggered backward half), reset at phase end
# baseline (speedup 1.0000x reference)
; #define LAS __attribute__((address_space(3)))
; template <bool FINAL> __device__ __forceinline__ void rglru_pass(Frame& F) {
;     const bf16* Z1 = WSP(const bf16, WS_Z); const bf16* WGT = WSP(const bf16, WS_WGT); bf16* AO = WSP(bf16, WS_AO);
;     float* SUM = WSP(float, WS_SUM);
;     const float* cw = F.in[20]; const float* cb = F.in[21];
;     LAS unsigned char* XCB = F.lds;
;     LAS float* XCF = (LAS float*)(F.lds + 17408);
;     LAS float* HS = (LAS float*)(F.lds + 17408 + 32768);
;     const int bx = blockIdx.x, h = bx & 15, cg = bx >> 4, ncg = F.G >> 4;
;     if (cg >= ncg) return;
;     const int r = F.lane & 31, hh = F.lane >> 5, jg = F.wave & 3, z = F.wave >> 2;
;     const int chl = 32 * jg + r, ch = h * 128 + chl;
.LBB0_1351:
	s_cmp_lt_u32 s94, 4
	s_cbranch_scc1 .Lprio_rg0
	s_setprio 1

; #define SEAM(k) do { if (IN(k) && IN((k) + 1)) { if ((MK_TAIL_MASK >> (k)) & 1u) moe_pull(F, (k), 0); if ((k) == 9) moe_pull(F, -1, NQ_LATE); if ((k) == 15) moe_pull(F, -1, NQ); xcd_barrier(bar); { int t_ = threadIdx.x; asm volatile("" : "+v"(t_)); F.tid = t_; F.lane = t_ & 63; } } } while (0)
; __device__ __forceinline__ void xcd_barrier(const XcdBarrier& b) {
;     asm volatile("s_waitcnt vmcnt(0)" ::: "memory");
;     __syncthreads();
;     if (threadIdx.x == 0) {
;         unsigned* bar = b.bar;
;         __builtin_amdgcn_s_waitcnt(0);
;         unsigned nloc = b.st[0], nx = b.st[1];
;         if (nloc == 0u) { xcd_barrier_complete(bar, b.x, b.total, nloc, nx); b.st[0] = nloc; b.st[1] = nx; }
; __global__ void __launch_bounds__(NWAVES * 64, 2) fwd_kernel(Args args) {
;     ...
;     if (IN(11)) { rglru_pass<false>(F); } SEAM(11);
.LBB0_1472:
	s_setprio 0
	s_cmp_gt_u32 s91, 12
	s_cselect_b64 s[0:1], -1, 0
	s_and_b64 s[0:1], s[10:11], s[0:1]
	s_andn2_b64 vcc, exec, s[0:1]
	s_cbranch_vccnz .LBB0_1526
	s_waitcnt vmcnt(0)
	s_waitcnt vmcnt(0) lgkmcnt(0)
	s_barrier
	s_mov_b64 s[0:1], exec
	v_readlane_b32 s2, v250, 59
	v_readlane_b32 s3, v250, 60
	s_and_b64 s[2:3], s[0:1], s[2:3]
	s_mov_b64 exec, s[2:3]
	s_cbranch_execz .LBB0_1525
	s_add_i32 s2, 0, 0x25020
	v_mov_b32_e32 v1, s2
	s_waitcnt vmcnt(0) expcnt(0) lgkmcnt(0)
	ds_read_b32 v3, v1
	s_add_i32 s2, 0, 0x25024
	v_mov_b32_e32 v1, s2
	ds_read_b32 v1, v1
	s_waitcnt lgkmcnt(1)
	v_cmp_ne_u32_e32 vcc, 0, v3
	s_cbranch_vccnz .LBB0_1489
	s_add_u32 s2, s88, 0x4200
	s_addc_u32 s3, s89, 0
	s_add_u32 s4, s88, 0x4400
	s_addc_u32 s5, s89, 0
	s_add_u32 s6, s88, 0x4500
	s_addc_u32 s7, s89, 0
	s_add_u32 s8, s88, 0x4600
	s_addc_u32 s9, s89, 0
	s_add_u32 s10, s88, 0x4700
	s_addc_u32 s11, s89, 0
	s_add_u32 s12, s88, 0x4800
	s_addc_u32 s13, s89, 0
	s_add_u32 s14, s88, 0x4900
	s_addc_u32 s15, s89, 0
	s_add_u32 s16, s88, 0x4a00
	s_addc_u32 s17, s89, 0
	s_add_u32 s18, s88, 0x4b00
	s_addc_u32 s19, s89, 0
	s_add_u32 s20, s88, 0x4c00
	s_addc_u32 s21, s89, 0
	s_add_u32 s22, s88, 0x4d00
	s_addc_u32 s23, s89, 0
	s_add_u32 s24, s88, 0x4e00
	s_addc_u32 s25, s89, 0
	s_add_u32 s26, s88, 0x4f00
	s_addc_u32 s27, s89, 0
	s_add_u32 s28, s88, 0x5000
	s_addc_u32 s29, s89, 0
	s_add_u32 s30, s88, 0x5100
	s_addc_u32 s31, s89, 0
	s_add_u32 s34, s88, 0x5200
	s_addc_u32 s35, s89, 0
	s_add_u32 s36, s88, 0x5300
	s_addc_u32 s37, s89, 0
	s_mov_b32 s33, 1
	v_mov_b32_e32 v17, 0
	s_branch .LBB0_1477

; #define SEAM(k) do { if (IN(k) && IN((k) + 1)) { if ((MK_TAIL_MASK >> (k)) & 1u) moe_pull(F, (k), 0); if ((k) == 9) moe_pull(F, -1, NQ_LATE); if ((k) == 15) moe_pull(F, -1, NQ); xcd_barrier(bar); { int t_ = threadIdx.x; asm volatile("" : "+v"(t_)); F.tid = t_; F.lane = t_ & 63; } } } while (0)
; __device__ __forceinline__ void xcd_barrier(const XcdBarrier& b) {
;     asm volatile("s_waitcnt vmcnt(0)" ::: "memory");
;     __syncthreads();
;     if (threadIdx.x == 0) {
;         unsigned* bar = b.bar;
;         __builtin_amdgcn_s_waitcnt(0);
;         unsigned nloc = b.st[0], nx = b.st[1];
;         if (nloc == 0u) { xcd_barrier_complete(bar, b.x, b.total, nloc, nx); b.st[0] = nloc; b.st[1] = nx; }
; __global__ void __launch_bounds__(NWAVES * 64, 2) fwd_kernel(Args args) {
;     ...
;     if (IN(13)) { rglru_pass<true>(F); } SEAM(13);
.LBB0_1607:
	s_setprio 0
	s_cmp_gt_i32 s91, 14
	s_cselect_b64 s[0:1], -1, 0
	s_and_b64 s[2:3], s[10:11], s[0:1]
	s_andn2_b64 vcc, exec, s[2:3]
	s_cbranch_vccnz .LBB0_1661
	s_waitcnt vmcnt(0)
	s_waitcnt vmcnt(0) lgkmcnt(0)
	s_barrier
	s_mov_b64 s[2:3], exec
	v_readlane_b32 s4, v250, 59
	v_readlane_b32 s5, v250, 60
	s_and_b64 s[4:5], s[2:3], s[4:5]
	s_mov_b64 exec, s[4:5]
	s_cbranch_execz .LBB0_1660
	s_add_i32 s4, 0, 0x25020
	v_mov_b32_e32 v1, s4
	s_waitcnt vmcnt(0) expcnt(0) lgkmcnt(0)
	ds_read_b32 v3, v1
	s_add_i32 s4, 0, 0x25024
	v_mov_b32_e32 v1, s4
	ds_read_b32 v1, v1
	s_waitcnt lgkmcnt(1)
	v_cmp_ne_u32_e32 vcc, 0, v3
	s_cbranch_vccnz .LBB0_1624
	s_add_u32 s4, s88, 0x4200
	s_addc_u32 s5, s89, 0
	s_add_u32 s6, s88, 0x4400
	s_addc_u32 s7, s89, 0
	s_add_u32 s8, s88, 0x4500
	s_addc_u32 s9, s89, 0
	s_add_u32 s10, s88, 0x4600
	s_addc_u32 s11, s89, 0
	s_add_u32 s12, s88, 0x4700
	s_addc_u32 s13, s89, 0
	s_add_u32 s14, s88, 0x4800
	s_addc_u32 s15, s89, 0
	s_add_u32 s16, s88, 0x4900
	s_addc_u32 s17, s89, 0
	s_add_u32 s18, s88, 0x4a00
	s_addc_u32 s19, s89, 0
	s_add_u32 s20, s88, 0x4b00
	s_addc_u32 s21, s89, 0
	s_add_u32 s22, s88, 0x4c00
	s_addc_u32 s23, s89, 0
	s_add_u32 s24, s88, 0x4d00
	s_addc_u32 s25, s89, 0
	s_add_u32 s26, s88, 0x4e00
	s_addc_u32 s27, s89, 0
	s_add_u32 s28, s88, 0x4f00
	s_addc_u32 s29, s89, 0
	s_add_u32 s30, s88, 0x5000
	s_addc_u32 s31, s89, 0
	s_add_u32 s34, s88, 0x5100
	s_addc_u32 s35, s89, 0
	s_add_u32 s36, s88, 0x5200
	s_addc_u32 s37, s89, 0
	s_add_u32 s38, s88, 0x5300
	s_addc_u32 s39, s89, 0
	s_mov_b32 s33, 1
	v_mov_b32_e32 v17, 0
	s_branch .LBB0_1612
